# dilated-attention band masks folded into the bias table; dead m0 save/restore removed around attention LDS-DMA
# speedup vs baseline: 1.0186x; 1.0124x over previous
.LBB0_264:
	v_mul_hi_i32 v3, v2, s16
	v_lshrrev_b32_e32 v4, 31, v3
	v_ashrrev_i32_e32 v3, 5, v3
	v_add_u32_e32 v3, v3, v4
	v_mad_u64_u32 v[4:5], s[12:13], v3, s17, v[2:3]
	v_cmp_gt_i32_e32 vcc, s18, v4
	v_mov_b32_e32 v5, 0xff800000
	s_and_saveexec_b64 s[12:13], vcc
	s_cbranch_execz .LBB0_263
	v_and_b32_e32 v5, -4, v3
	v_cmp_eq_u32_e32 vcc, 4, v5
	s_nop 1
	v_cndmask_b32_e64 v5, 4, 2, vcc
	v_cmp_lt_u32_e32 vcc, 3, v3
	s_nop 1
	v_cndmask_b32_e32 v5, 0, v5, vcc
	v_lshlrev_b32_e32 v4, v5, v4
	v_cmp_lt_i32_e32 vcc, 15, v4
	s_and_saveexec_b64 s[14:15], vcc
	s_cbranch_execz .LBB0_262
	v_cvt_f32_u32_e32 v4, v4
	v_mul_f32_e32 v4, 0x3d800000, v4
	v_cmp_gt_f32_e32 vcc, s19, v4
	s_nop 1
	v_cndmask_b32_e64 v5, 0, 32, vcc
	v_ldexp_f32 v4, v4, v5
	v_log_f32_e32 v4, v4
	v_cndmask_b32_e32 v5, 0, v6, vcc
	v_mul_f32_e32 v7, 0x3f317217, v4
	v_fma_f32 v7, v4, s23, -v7
	v_fmac_f32_e32 v7, 0x3377d1cf, v4
	v_fmac_f32_e32 v7, 0x3f317217, v4
	v_cmp_lt_f32_e64 vcc, |v4|, s24
	s_nop 1
	v_cndmask_b32_e32 v4, v4, v7, vcc
	v_sub_f32_e32 v4, v4, v5
	v_div_scale_f32 v5, s[30:31], s25, s25, v4
	v_rcp_f32_e32 v7, v5
	v_div_scale_f32 v10, vcc, v4, s25, v4
	v_fma_f32 v11, -v5, v7, 1.0
	v_fmac_f32_e32 v7, v11, v7
	v_mul_f32_e32 v11, v10, v7
	v_fma_f32 v12, -v5, v11, v10
	v_fmac_f32_e32 v11, v12, v7
	v_fma_f32 v5, -v5, v11, v10
	v_div_fmas_f32 v5, v5, v7, v11
	v_div_fixup_f32 v4, v5, s25, v4
	v_mul_f32_e32 v4, 0x41800000, v4
	v_cvt_i32_f32_e32 v4, v4
	v_min_i32_e32 v4, 15, v4
	v_add_u32_e32 v4, 16, v4
	s_branch .LBB0_262

.LBB0_1520:
	s_or_b64 exec, exec, s[34:35]
	s_ashr_i32 s50, s41, 6
	s_lshl_b32 s51, s82, 8
	s_lshl_b32 s46, s50, 5
	s_lshl_b32 s36, s83, 11
	s_add_i32 s46, s46, s51
	s_and_b64 s[34:35], s[4:5], exec
	s_movk_i32 s34, 0x80
	s_cselect_b32 s37, 0x200, s34
	s_and_b64 s[34:35], s[10:11], exec
	v_and_b32_e32 v138, 31, v4
	s_cselect_b32 s47, 0x800, s37
	s_and_b64 s[4:5], s[4:5], exec
	v_or_b32_e32 v136, s46, v138
	s_cselect_b32 s34, 2, 4
	s_and_b64 s[4:5], s[10:11], exec
	v_cmp_gt_i32_e32 vcc, s47, v136
	s_cselect_b32 s45, 0, s34
	s_lshl_b32 s4, s40, 23
	v_cndmask_b32_e32 v2, 0, v136, vcc
	s_add_u32 s4, s16, s4
	v_lshlrev_b32_e32 v2, s45, v2
	s_addc_u32 s5, s17, 0
	s_or_b32 s35, s36, s7
	v_add_u32_e32 v8, s35, v2
	v_ashrrev_i32_e32 v9, 31, v8
	v_lshlrev_b64 v[8:9], 9, v[8:9]
	v_bfe_u32 v6, v4, 5, 1
	v_lshl_add_u64 v[8:9], s[4:5], 0, v[8:9]
	s_lshl_b32 s48, s6, 7
	v_lshl_add_u64 v[8:9], v[8:9], 0, s[48:49]
	v_lshlrev_b32_e32 v2, 4, v6
	v_lshl_add_u64 v[8:9], v[8:9], 0, v[2:3]
	s_mov_b64 s[10:11], 0x4000000
	v_lshl_add_u64 v[132:133], v[8:9], 0, s[10:11]
	v_add_co_u32_e32 v8, vcc, 0x4000000, v8
	s_movk_i32 s10, 0x100
	s_nop 0
	v_addc_co_u32_e32 v9, vcc, 0, v9, vcc
	global_load_dwordx4 v[116:119], v[132:133], off offset:32
	global_load_dwordx4 v[120:123], v[132:133], off offset:64
	global_load_dwordx4 v[124:127], v[8:9], off
	global_load_dwordx4 v[128:131], v[132:133], off offset:96
	s_lshl_b32 s34, s40, 2
	v_cmp_gt_i32_e32 vcc, s10, v4
	s_and_saveexec_b64 s[10:11], vcc
	s_cbranch_execz .LBB0_1524
	v_cmp_lt_i32_e32 vcc, 63, v4
	v_mov_b32_e32 v2, 0xff800000
	s_and_saveexec_b64 s[38:39], vcc
	s_cbranch_execz .LBB0_1523
	s_or_b32 s37, s34, s6
	s_mul_i32 s48, s37, 0xc0
	s_lshl_b64 s[40:41], s[48:49], 2
	s_add_u32 s40, s0, s40
	s_addc_u32 s41, s1, s41
	v_mov_b32_e32 v5, v3
	v_lshl_add_u64 v[8:9], v[4:5], 2, s[40:41]
	v_add_co_u32_e32 v8, vcc, 0x129000, v8
	s_nop 1
	v_addc_co_u32_e32 v9, vcc, 0, v9, vcc
	global_load_dword v2, v[8:9], off offset:768

.LBB0_1524:
	s_or_b64 exec, exec, s[10:11]
	s_waitcnt lgkmcnt(0)
	s_barrier
	s_waitcnt vmcnt(0)
	v_and_b32_e32 v137, 63, v4
	s_lshl_b32 s38, s6, 6
	s_waitcnt vmcnt(1)
	s_waitcnt vmcnt(0)
	s_and_saveexec_b64 s[10:11], s[12:13]
	v_mov_b32_e32 v2, s69
	ds_write_b32 v2, v7
	s_or_b64 exec, exec, s[10:11]
	s_ashr_i32 s37, s36, 31
	s_lshl_b64 s[10:11], s[36:37], 9
	s_add_u32 s4, s4, s10
	s_addc_u32 s5, s5, s11
	s_lshl_b32 s10, s38, 1
	s_add_u32 s4, s4, s10
	s_addc_u32 s5, s5, 0
	s_add_u32 s10, s4, 0x7000000
	s_addc_u32 s11, s5, 0
	s_add_i32 s48, s51, 0xffffff80
	s_add_u32 s4, s4, 0x5800000
	s_addc_u32 s5, s5, 0
	s_cmp_eq_u32 s82, 0
	s_cselect_b32 s61, 2, 0
	s_or_b32 s59, s61, 1
	s_add_i32 s52, s61, 2
	s_cmp_le_u32 s52, s44
	s_cselect_b64 s[40:41], -1, 0
	s_add_i32 s12, s61, 3
	s_cmp_gt_u32 s52, s44
	s_cselect_b32 s53, s52, s12
	s_lshl_b32 s38, s61, 6
	s_add_i32 s57, s38, s48
	v_or_b32_e32 v2, s57, v137
	v_max_i32_e32 v2, 0, v2
	v_lshlrev_b32_e32 v2, s45, v2
	v_add_u32_e32 v4, s7, v2
	v_ashrrev_i32_e32 v5, 31, v4
	s_lshl_b32 s36, s50, 3
	v_lshlrev_b64 v[4:5], 9, v[4:5]
	s_ashr_i32 s37, s36, 31
	v_lshl_add_u64 v[4:5], s[4:5], 0, v[4:5]
	s_lshl_b64 s[12:13], s[36:37], 1
	s_lshl_b32 s58, s50, 10
	v_lshl_add_u64 v[4:5], v[4:5], 0, s[12:13]
	s_add_i32 s54, s58, s68
	s_mov_b32 m0, s54
	s_nop 0
	global_load_lds_dwordx4 v[4:5], off
	s_lshl_b32 s39, s59, 6
	s_add_i32 s60, s39, s48
	v_or_b32_e32 v2, s60, v137
	v_max_i32_e32 v2, 0, v2
	v_lshlrev_b32_e32 v2, s45, v2
	v_add_u32_e32 v4, s7, v2
	v_ashrrev_i32_e32 v5, 31, v4
	v_lshlrev_b64 v[4:5], 9, v[4:5]
	v_lshl_add_u64 v[4:5], s[4:5], 0, v[4:5]
	v_lshl_add_u64 v[4:5], v[4:5], 0, s[12:13]
	s_add_i32 s39, s58, s71
	v_lshrrev_b32_e32 v7, 2, v137
	s_mov_b32 m0, s39
	s_nop 0
	global_load_lds_dwordx4 v[4:5], off
	s_lshl_b32 s39, s50, 4
	v_or_b32_e32 v4, s48, v7
	s_and_b32 s56, s39, 48
	v_add_u32_e32 v2, s38, v4
	v_or_b32_e32 v2, s56, v2
	v_max_i32_e32 v2, 0, v2
	v_lshlrev_b32_e32 v2, s45, v2
	v_add_u32_e32 v8, s7, v2
	v_ashrrev_i32_e32 v9, 31, v8
	v_lshlrev_b64 v[8:9], 9, v[8:9]
	s_and_b32 s38, s36, 0xffffffe0
	v_lshlrev_b32_e32 v2, 3, v137
	v_lshl_add_u64 v[8:9], s[10:11], 0, v[8:9]
	s_ashr_i32 s39, s38, 31
	v_and_b32_e32 v5, 24, v2
	v_lshl_add_u64 v[8:9], s[38:39], 1, v[8:9]
	v_lshlrev_b32_e32 v2, 1, v5
	v_lshl_add_u64 v[8:9], v[8:9], 0, v[2:3]
	s_add_i32 s55, s58, s72
	s_mov_b32 m0, s55
	s_nop 0
	global_load_lds_dwordx4 v[8:9], off
	v_or_b32_e32 v7, s60, v7
	s_mov_b64 s[42:43], -1
	s_cmp_gt_u32 s53, s44
	v_or_b32_e32 v7, s56, v7
	s_cbranch_scc1 .LBB0_1528
	s_lshl_b32 s60, s52, 6
	s_add_i32 s42, s60, s48
	v_or_b32_e32 v8, s42, v137
	v_lshlrev_b32_e32 v8, s45, v8
	v_add_u32_e32 v8, s7, v8
	v_ashrrev_i32_e32 v9, 31, v8
	v_lshlrev_b64 v[8:9], 9, v[8:9]
	v_lshl_add_u64 v[8:9], s[4:5], 0, v[8:9]
	v_lshl_add_u64 v[8:9], v[8:9], 0, s[12:13]
	s_add_i32 s42, s58, s73
	s_mov_b32 m0, s42
	s_nop 0
	global_load_lds_dwordx4 v[8:9], off
	v_max_i32_e32 v8, 0, v7
	v_lshlrev_b32_e32 v8, s45, v8
	v_add_u32_e32 v8, s7, v8
	v_ashrrev_i32_e32 v9, 31, v8
	v_lshlrev_b64 v[8:9], 9, v[8:9]
	v_lshl_add_u64 v[8:9], s[10:11], 0, v[8:9]
	s_lshl_b64 s[42:43], s[38:39], 1
	v_lshl_add_u64 v[8:9], v[8:9], 0, s[42:43]
	s_add_i32 s62, s58, s76
	v_lshl_add_u64 v[8:9], v[8:9], 0, v[2:3]
	s_mov_b32 m0, s62
	s_nop 0
	global_load_lds_dwordx4 v[8:9], off
	s_lshl_b32 s62, s53, 6
	s_add_i32 s62, s62, s48
	v_or_b32_e32 v8, s62, v137
	v_lshlrev_b32_e32 v8, s45, v8
	v_add_u32_e32 v8, s7, v8
	v_ashrrev_i32_e32 v9, 31, v8
	v_lshlrev_b64 v[8:9], 9, v[8:9]
	v_lshl_add_u64 v[8:9], s[4:5], 0, v[8:9]
	v_lshl_add_u64 v[8:9], v[8:9], 0, s[12:13]
	s_add_i32 s62, s58, s77
	s_mov_b32 m0, s62
	s_nop 0
	global_load_lds_dwordx4 v[8:9], off
	v_add_u32_e32 v8, s60, v4
	v_or_b32_e32 v8, s56, v8
	v_max_i32_e32 v8, 0, v8
	v_lshlrev_b32_e32 v8, s45, v8
	v_add_u32_e32 v8, s7, v8
	v_ashrrev_i32_e32 v9, 31, v8
	v_lshlrev_b64 v[8:9], 9, v[8:9]
	v_lshl_add_u64 v[8:9], s[10:11], 0, v[8:9]
	v_lshl_add_u64 v[8:9], v[8:9], 0, s[42:43]
	v_lshl_add_u64 v[8:9], v[8:9], 0, v[2:3]
	s_add_i32 s42, s58, s78
	s_mov_b32 m0, s42
	s_nop 0
	global_load_lds_dwordx4 v[8:9], off
	s_waitcnt vmcnt(4) lgkmcnt(0)
	s_barrier
	s_mov_b64 s[42:43], 0
.LBB0_1528:
	s_andn2_b64 vcc, exec, s[42:43]
	s_cbranch_vccnz .LBB0_1534
	s_andn2_b64 vcc, exec, s[40:41]
	s_mov_b64 s[40:41], -1
	s_cbranch_vccnz .LBB0_1531
	s_lshl_b32 s40, s52, 6
	s_add_i32 s41, s40, s48
	v_or_b32_e32 v8, s41, v137
	v_lshlrev_b32_e32 v8, s45, v8
	v_add_u32_e32 v8, s7, v8
	v_ashrrev_i32_e32 v9, 31, v8
	v_lshlrev_b64 v[8:9], 9, v[8:9]
	v_lshl_add_u64 v[8:9], s[4:5], 0, v[8:9]
	v_lshl_add_u64 v[8:9], s[36:37], 1, v[8:9]
	s_add_i32 s36, s58, s73
	s_mov_b32 m0, s36
	s_nop 0
	global_load_lds_dwordx4 v[8:9], off
	v_max_i32_e32 v8, 0, v7
	v_lshlrev_b32_e32 v8, s45, v8
	v_add_u32_e32 v8, s7, v8
	v_ashrrev_i32_e32 v9, 31, v8
	v_lshlrev_b64 v[8:9], 9, v[8:9]
	v_lshl_add_u64 v[8:9], s[10:11], 0, v[8:9]
	s_lshl_b64 s[36:37], s[38:39], 1
	v_lshl_add_u64 v[8:9], v[8:9], 0, s[36:37]
	v_lshl_add_u64 v[8:9], v[8:9], 0, v[2:3]
	s_add_i32 s41, s58, s76
	s_mov_b32 m0, s41
	s_nop 0
	global_load_lds_dwordx4 v[8:9], off
	v_add_u32_e32 v8, s40, v4
	v_or_b32_e32 v8, s56, v8
	v_max_i32_e32 v8, 0, v8
	v_lshlrev_b32_e32 v8, s45, v8
	v_add_u32_e32 v8, s7, v8
	v_ashrrev_i32_e32 v9, 31, v8
	v_lshlrev_b64 v[8:9], 9, v[8:9]
	v_lshl_add_u64 v[8:9], s[10:11], 0, v[8:9]
	v_lshl_add_u64 v[8:9], v[8:9], 0, s[36:37]
	v_lshl_add_u64 v[8:9], v[8:9], 0, v[2:3]
	s_add_i32 s36, s58, s78
	s_mov_b32 m0, s36
	s_nop 0
	global_load_lds_dwordx4 v[8:9], off
	s_mov_b64 s[40:41], 0
.LBB0_1531:
	s_andn2_b64 vcc, exec, s[40:41]
	s_cbranch_vccnz .LBB0_1533
	v_max_i32_e32 v7, 0, v7
	v_lshlrev_b32_e32 v7, s45, v7
	v_add_u32_e32 v8, s7, v7
	v_ashrrev_i32_e32 v9, 31, v8
	v_lshlrev_b64 v[8:9], 9, v[8:9]
	v_lshl_add_u64 v[8:9], s[10:11], 0, v[8:9]
	v_lshl_add_u64 v[8:9], s[38:39], 1, v[8:9]
	v_lshl_add_u64 v[8:9], v[8:9], 0, v[2:3]
	s_add_i32 s36, s58, s76
	s_mov_b32 m0, s36
	s_nop 0
	global_load_lds_dwordx4 v[8:9], off

.LBB0_1543:
	s_cmp_le_i32 s53, s44
	s_cselect_b64 s[10:11], -1, 0
	s_cmp_lg_u64 s[10:11], 0
	s_addc_u32 s58, s53, 0
	s_add_i32 s4, s57, -1
	s_and_b32 s42, s4, 3
	s_cmp_le_i32 s58, s44
	s_cselect_b64 s[40:41], -1, 0
	s_cmp_gt_i32 s58, s44
	s_cselect_b64 s[4:5], -1, 0
	s_mov_b64 s[12:13], -1
	s_and_b64 vcc, exec, s[4:5]
	s_cbranch_vccz .LBB0_1547
	s_andn2_b64 vcc, exec, s[10:11]
	s_cbranch_vccnz .LBB0_1546
	v_lshl_add_u32 v2, s53, 6, v139
	v_max_i32_e32 v2, 0, v2
	v_lshlrev_b32_e32 v2, s45, v2
	v_add_u32_e32 v146, s7, v2
	v_ashrrev_i32_e32 v147, 31, v146
	v_lshlrev_b64 v[146:147], 9, v[146:147]
	s_lshl_b32 s10, s42, 13
	v_lshl_add_u64 v[146:147], v[134:135], 0, v[146:147]
	s_add_i32 s10, s10, s55
	s_mov_b32 m0, s10
	s_nop 0
	global_load_lds_dwordx4 v[146:147], off

.LBB0_1547:
	s_andn2_b64 vcc, exec, s[12:13]
	s_cbranch_vccnz .LBB0_1549
	v_lshl_add_u32 v2, s58, 6, v140
	v_max_i32_e32 v2, 0, v2
	v_lshlrev_b32_e32 v2, s45, v2
	v_add_u32_e32 v146, s7, v2
	v_ashrrev_i32_e32 v147, 31, v146
	v_lshl_add_u32 v2, s53, 6, v139
	v_lshlrev_b64 v[146:147], 9, v[146:147]
	v_max_i32_e32 v2, 0, v2
	v_lshl_add_u64 v[146:147], s[38:39], 0, v[146:147]
	s_lshl_b32 s10, s56, 13
	v_lshlrev_b32_e32 v2, s45, v2
	s_add_i32 s10, s10, s54
	s_mov_b32 m0, s10
	s_nop 0
	global_load_lds_dwordx4 v[146:147], off
	v_add_u32_e32 v146, s7, v2
	v_ashrrev_i32_e32 v147, 31, v146
	v_lshlrev_b64 v[146:147], 9, v[146:147]
	s_lshl_b32 s10, s42, 13
	v_lshl_add_u64 v[146:147], v[134:135], 0, v[146:147]
	s_add_i32 s10, s10, s55
	s_mov_b32 m0, s10
	s_nop 0
	global_load_lds_dwordx4 v[146:147], off

.LBB0_1560:
	s_cmp_eq_u32 s63, 3
	s_cselect_b64 s[12:13], -1, 0
	s_cmp_eq_u32 s62, 3
	s_cselect_b64 s[46:47], -1, 0
	s_and_b64 s[12:13], s[12:13], s[46:47]
	s_and_b64 vcc, exec, s[12:13]
	s_cbranch_vccnz .LBB0_1566
	s_lshl_b32 s12, s61, 6
	s_add_i32 s12, s12, s51
	s_lshl_b32 s12, s12, 2
	v_subrev_u32_e32 v2, s12, v143
	ds_read2_b32 v[146:147], v2 offset0:127 offset1:128
	s_or_b32 s12, s62, s63
	s_cmp_eq_u32 s12, 0
	s_waitcnt lgkmcnt(0)
	v_pk_add_f32 v[68:69], v[68:69], v[146:147] op_sel:[0,1] op_sel_hi:[1,0]
	ds_read2_b32 v[146:147], v2 offset0:95 offset1:96
	s_waitcnt lgkmcnt(0)
	v_pk_add_f32 v[36:37], v[36:37], v[146:147] op_sel:[0,1] op_sel_hi:[1,0]
	ds_read2_b32 v[146:147], v2 offset0:125 offset1:126
	s_waitcnt lgkmcnt(0)
	v_pk_add_f32 v[70:71], v[70:71], v[146:147] op_sel:[0,1] op_sel_hi:[1,0]
	ds_read2_b32 v[146:147], v2 offset0:93 offset1:94
	s_waitcnt lgkmcnt(0)
	v_pk_add_f32 v[38:39], v[38:39], v[146:147] op_sel:[0,1] op_sel_hi:[1,0]
	ds_read2_b32 v[146:147], v2 offset0:119 offset1:120
	s_waitcnt lgkmcnt(0)
	v_pk_add_f32 v[72:73], v[72:73], v[146:147] op_sel:[0,1] op_sel_hi:[1,0]
	ds_read2_b32 v[146:147], v2 offset0:87 offset1:88
	s_waitcnt lgkmcnt(0)
	v_pk_add_f32 v[40:41], v[40:41], v[146:147] op_sel:[0,1] op_sel_hi:[1,0]
	ds_read2_b32 v[146:147], v2 offset0:117 offset1:118
	s_waitcnt lgkmcnt(0)
	v_pk_add_f32 v[74:75], v[74:75], v[146:147] op_sel:[0,1] op_sel_hi:[1,0]
	ds_read2_b32 v[146:147], v2 offset0:85 offset1:86
	s_waitcnt lgkmcnt(0)
	v_pk_add_f32 v[42:43], v[42:43], v[146:147] op_sel:[0,1] op_sel_hi:[1,0]
	ds_read2_b32 v[146:147], v2 offset0:111 offset1:112
	s_waitcnt lgkmcnt(0)
	v_pk_add_f32 v[76:77], v[76:77], v[146:147] op_sel:[0,1] op_sel_hi:[1,0]
	ds_read2_b32 v[146:147], v2 offset0:79 offset1:80
	s_waitcnt lgkmcnt(0)
	v_pk_add_f32 v[44:45], v[44:45], v[146:147] op_sel:[0,1] op_sel_hi:[1,0]
	ds_read2_b32 v[146:147], v2 offset0:109 offset1:110
	s_waitcnt lgkmcnt(0)
	v_pk_add_f32 v[78:79], v[78:79], v[146:147] op_sel:[0,1] op_sel_hi:[1,0]
	ds_read2_b32 v[146:147], v2 offset0:77 offset1:78
	s_waitcnt lgkmcnt(0)
	v_pk_add_f32 v[46:47], v[46:47], v[146:147] op_sel:[0,1] op_sel_hi:[1,0]
	ds_read2_b32 v[146:147], v2 offset0:103 offset1:104
	s_waitcnt lgkmcnt(0)
	v_pk_add_f32 v[80:81], v[80:81], v[146:147] op_sel:[0,1] op_sel_hi:[1,0]
	ds_read2_b32 v[146:147], v2 offset0:71 offset1:72
	s_waitcnt lgkmcnt(0)
	v_pk_add_f32 v[48:49], v[48:49], v[146:147] op_sel:[0,1] op_sel_hi:[1,0]
	ds_read2_b32 v[146:147], v2 offset0:101 offset1:102
	s_waitcnt lgkmcnt(0)
	v_pk_add_f32 v[82:83], v[82:83], v[146:147] op_sel:[0,1] op_sel_hi:[1,0]
	ds_read2_b32 v[146:147], v2 offset0:69 offset1:70
	s_waitcnt lgkmcnt(0)
	v_pk_add_f32 v[50:51], v[50:51], v[146:147] op_sel:[0,1] op_sel_hi:[1,0]
	s_branch .LBB0_1563
	s_cmp_eq_u32 s63, 2
	s_cselect_b64 vcc, -1, 0
	s_cmp_eq_u32 s63, 1
	s_cselect_b64 s[12:13], -1, 0
	s_cmp_eq_u32 s63, 3
	s_cselect_b32 s46, 64, 0
	v_mov_b32_e32 v2, s46
	s_cselect_b32 s46, -1, 63
	s_cmp_eq_u32 s62, 2
	v_cndmask_b32_e32 v2, v2, v138, vcc
	v_mov_b32_e32 v146, s46
	s_cselect_b64 vcc, -1, 0
	s_cmp_eq_u32 s62, 1
	v_cndmask_b32_e64 v146, v146, v138, s[12:13]
	s_cselect_b64 s[12:13], -1, 0
	s_cmp_eq_u32 s62, 3
	s_cselect_b32 s46, 64, 0
	v_mov_b32_e32 v147, s46
	s_cselect_b32 s46, -1, 63
	v_sub_u32_e32 v2, v2, v141
	v_sub_u32_e32 v146, v146, v141
	v_mov_b32_e32 v148, s46
	v_cndmask_b32_e32 v147, v147, v138, vcc
	v_cndmask_b32_e64 v148, v148, v138, s[12:13]
	v_cmp_lt_i32_e32 vcc, 0, v2
	v_cmp_gt_i32_e64 s[12:13], 0, v146
	v_sub_u32_e32 v147, v147, v141
	v_sub_u32_e32 v148, v148, v141
	s_or_b64 vcc, vcc, s[12:13]
	v_cndmask_b32_e32 v68, v68, v234, vcc
	v_cmp_lt_i32_e32 vcc, 0, v147
	v_cmp_gt_i32_e64 s[12:13], 0, v148
	s_or_b64 vcc, vcc, s[12:13]
	v_cndmask_b32_e32 v36, v36, v234, vcc
	v_cmp_lt_i32_e32 vcc, 1, v2
	v_cmp_gt_i32_e64 s[12:13], 1, v146
	s_or_b64 vcc, vcc, s[12:13]
	v_cndmask_b32_e32 v69, v69, v234, vcc
	v_cmp_lt_i32_e32 vcc, 1, v147
	v_cmp_gt_i32_e64 s[12:13], 1, v148
	s_or_b64 vcc, vcc, s[12:13]
	v_cndmask_b32_e32 v37, v37, v234, vcc
	v_cmp_lt_i32_e32 vcc, 2, v2
	v_cmp_gt_i32_e64 s[12:13], 2, v146
	s_or_b64 vcc, vcc, s[12:13]
	v_cndmask_b32_e32 v70, v70, v234, vcc
	v_cmp_lt_i32_e32 vcc, 2, v147
	v_cmp_gt_i32_e64 s[12:13], 2, v148
	s_or_b64 vcc, vcc, s[12:13]
	v_cndmask_b32_e32 v38, v38, v234, vcc
	v_cmp_lt_i32_e32 vcc, 3, v2
	v_cmp_gt_i32_e64 s[12:13], 3, v146
	s_or_b64 vcc, vcc, s[12:13]
	v_cndmask_b32_e32 v71, v71, v234, vcc
	v_cmp_lt_i32_e32 vcc, 3, v147
	v_cmp_gt_i32_e64 s[12:13], 3, v148
	s_or_b64 vcc, vcc, s[12:13]
	v_cndmask_b32_e32 v39, v39, v234, vcc
	v_cmp_lt_i32_e32 vcc, 8, v2
	v_cmp_gt_i32_e64 s[12:13], 8, v146
	s_or_b64 vcc, vcc, s[12:13]
	v_cndmask_b32_e32 v72, v72, v234, vcc
	v_cmp_lt_i32_e32 vcc, 8, v147
	v_cmp_gt_i32_e64 s[12:13], 8, v148
	s_or_b64 vcc, vcc, s[12:13]
	v_cndmask_b32_e32 v40, v40, v234, vcc
	v_cmp_lt_i32_e32 vcc, 9, v2
	v_cmp_gt_i32_e64 s[12:13], 9, v146
	s_or_b64 vcc, vcc, s[12:13]
	v_cndmask_b32_e32 v73, v73, v234, vcc
	v_cmp_lt_i32_e32 vcc, 9, v147
	v_cmp_gt_i32_e64 s[12:13], 9, v148
	s_or_b64 vcc, vcc, s[12:13]
	v_cndmask_b32_e32 v41, v41, v234, vcc
	v_cmp_lt_i32_e32 vcc, 10, v2
	v_cmp_gt_i32_e64 s[12:13], 10, v146
	s_or_b64 vcc, vcc, s[12:13]
	v_cndmask_b32_e32 v74, v74, v234, vcc
	v_cmp_lt_i32_e32 vcc, 10, v147
	v_cmp_gt_i32_e64 s[12:13], 10, v148
	s_or_b64 vcc, vcc, s[12:13]
	v_cndmask_b32_e32 v42, v42, v234, vcc
	v_cmp_lt_i32_e32 vcc, 11, v2
	v_cmp_gt_i32_e64 s[12:13], 11, v146
	s_or_b64 vcc, vcc, s[12:13]
	v_cndmask_b32_e32 v75, v75, v234, vcc
	v_cmp_lt_i32_e32 vcc, 11, v147
	v_cmp_gt_i32_e64 s[12:13], 11, v148
	s_or_b64 vcc, vcc, s[12:13]
	v_cndmask_b32_e32 v43, v43, v234, vcc
	v_cmp_lt_i32_e32 vcc, 16, v2
	v_cmp_gt_i32_e64 s[12:13], 16, v146
	s_or_b64 vcc, vcc, s[12:13]
	v_cndmask_b32_e32 v76, v76, v234, vcc
	v_cmp_lt_i32_e32 vcc, 16, v147
	v_cmp_gt_i32_e64 s[12:13], 16, v148
	s_or_b64 vcc, vcc, s[12:13]
	v_cndmask_b32_e32 v44, v44, v234, vcc
	v_cmp_lt_i32_e32 vcc, 17, v2
	v_cmp_gt_i32_e64 s[12:13], 17, v146
	s_or_b64 vcc, vcc, s[12:13]
	v_cndmask_b32_e32 v77, v77, v234, vcc
	v_cmp_lt_i32_e32 vcc, 17, v147
	v_cmp_gt_i32_e64 s[12:13], 17, v148
	s_or_b64 vcc, vcc, s[12:13]
	v_cndmask_b32_e32 v45, v45, v234, vcc
	v_cmp_lt_i32_e32 vcc, 18, v2
	v_cmp_gt_i32_e64 s[12:13], 18, v146
	s_or_b64 vcc, vcc, s[12:13]
	v_cndmask_b32_e32 v78, v78, v234, vcc
	v_cmp_lt_i32_e32 vcc, 18, v147
	v_cmp_gt_i32_e64 s[12:13], 18, v148
	s_or_b64 vcc, vcc, s[12:13]
	v_cndmask_b32_e32 v46, v46, v234, vcc
	v_cmp_lt_i32_e32 vcc, 19, v2
	v_cmp_gt_i32_e64 s[12:13], 19, v146
	s_or_b64 vcc, vcc, s[12:13]
	v_cndmask_b32_e32 v79, v79, v234, vcc
	v_cmp_lt_i32_e32 vcc, 19, v147
	v_cmp_gt_i32_e64 s[12:13], 19, v148
	s_or_b64 vcc, vcc, s[12:13]
	v_cndmask_b32_e32 v47, v47, v234, vcc
	v_cmp_lt_i32_e32 vcc, 24, v2
	v_cmp_gt_i32_e64 s[12:13], 24, v146
	s_or_b64 vcc, vcc, s[12:13]
	v_cndmask_b32_e32 v80, v80, v234, vcc
	v_cmp_lt_i32_e32 vcc, 24, v147
	v_cmp_gt_i32_e64 s[12:13], 24, v148
	s_or_b64 vcc, vcc, s[12:13]
	v_cndmask_b32_e32 v48, v48, v234, vcc
	v_cmp_lt_i32_e32 vcc, 25, v2
	v_cmp_gt_i32_e64 s[12:13], 25, v146
	s_or_b64 vcc, vcc, s[12:13]
	v_cndmask_b32_e32 v81, v81, v234, vcc
	v_cmp_lt_i32_e32 vcc, 25, v147
	v_cmp_gt_i32_e64 s[12:13], 25, v148
	s_or_b64 vcc, vcc, s[12:13]
	v_cndmask_b32_e32 v49, v49, v234, vcc
	v_cmp_lt_i32_e32 vcc, 26, v2
	v_cmp_gt_i32_e64 s[12:13], 26, v146
	s_or_b64 vcc, vcc, s[12:13]
	v_cndmask_b32_e32 v82, v82, v234, vcc
	v_cmp_lt_i32_e32 vcc, 26, v147
	v_cmp_gt_i32_e64 s[12:13], 26, v148
	s_or_b64 vcc, vcc, s[12:13]
	v_cndmask_b32_e32 v50, v50, v234, vcc
	v_cmp_lt_i32_e32 vcc, 27, v2
	v_cmp_gt_i32_e64 s[12:13], 27, v146
	s_or_b64 vcc, vcc, s[12:13]
	v_cndmask_b32_e32 v83, v83, v234, vcc
	v_cmp_lt_i32_e32 vcc, 27, v147
	v_cmp_gt_i32_e64 s[12:13], 27, v148
	s_or_b64 vcc, vcc, s[12:13]
	v_cndmask_b32_e32 v51, v51, v234, vcc

.LBB0_1572:
	v_cndmask_b32_e64 v145, 0, 1, s[40:41]
	s_mov_b64 s[12:13], -1
	v_readfirstlane_b32 s4, v145
	s_add_i32 s46, s58, s4
	s_cmp_le_i32 s46, s44
	s_cselect_b64 s[4:5], -1, 0
	s_cmp_gt_i32 s46, s44
	s_cbranch_scc1 .LBB0_1574
	v_lshl_add_u32 v145, s46, 6, v140
	v_max_i32_e32 v145, 0, v145
	v_lshlrev_b32_e32 v145, s45, v145
	v_add_u32_e32 v146, s7, v145
	v_ashrrev_i32_e32 v147, 31, v146
	v_lshl_add_u32 v145, s58, 6, v139
	v_lshlrev_b64 v[146:147], 9, v[146:147]
	v_max_i32_e32 v145, 0, v145
	v_lshl_add_u64 v[146:147], s[38:39], 0, v[146:147]
	s_lshl_b32 s12, s60, 13
	v_lshlrev_b32_e32 v145, s45, v145
	s_add_i32 s12, s12, s54
	s_mov_b32 m0, s12
	s_nop 0
	global_load_lds_dwordx4 v[146:147], off
	v_add_u32_e32 v146, s7, v145
	v_ashrrev_i32_e32 v147, 31, v146
	v_lshlrev_b64 v[146:147], 9, v[146:147]
	s_lshl_b32 s12, s57, 13
	v_lshl_add_u64 v[146:147], v[134:135], 0, v[146:147]
	s_add_i32 s12, s12, s55
	s_mov_b32 m0, s12
	s_nop 0
	global_load_lds_dwordx4 v[146:147], off
	s_mov_b64 s[12:13], 0
.LBB0_1574:
	s_andn2_b64 vcc, exec, s[12:13]
	s_cbranch_vccnz .LBB0_1577
	s_andn2_b64 vcc, exec, s[40:41]
	s_cbranch_vccnz .LBB0_1577
	v_lshl_add_u32 v145, s58, 6, v139
	v_max_i32_e32 v145, 0, v145
	v_lshlrev_b32_e32 v145, s45, v145
	v_add_u32_e32 v146, s7, v145
	v_ashrrev_i32_e32 v147, 31, v146
	v_lshlrev_b64 v[146:147], 9, v[146:147]
	s_lshl_b32 s12, s57, 13
	v_lshl_add_u64 v[146:147], v[134:135], 0, v[146:147]
	s_add_i32 s12, s12, s55
	s_mov_b32 m0, s12
	s_nop 0
	global_load_lds_dwordx4 v[146:147], off

.LBB0_1588:
	s_cmp_eq_u32 s60, 3
	s_cselect_b64 s[12:13], -1, 0
	s_cmp_eq_u32 s47, 3
	s_cselect_b64 s[40:41], -1, 0
	s_and_b64 s[12:13], s[12:13], s[40:41]
	s_and_b64 vcc, exec, s[12:13]
	s_cbranch_vccnz .LBB0_1594
	s_lshl_b32 s12, s59, 6
	s_add_i32 s12, s12, s51
	s_lshl_b32 s12, s12, 2
	v_subrev_u32_e32 v145, s12, v143
	ds_read2_b32 v[146:147], v145 offset0:127 offset1:128
	s_or_b32 s12, s47, s60
	s_cmp_eq_u32 s12, 0
	s_waitcnt lgkmcnt(0)
	v_pk_add_f32 v[84:85], v[84:85], v[146:147] op_sel:[0,1] op_sel_hi:[1,0]
	ds_read2_b32 v[146:147], v145 offset0:95 offset1:96
	s_waitcnt lgkmcnt(0)
	v_pk_add_f32 v[100:101], v[100:101], v[146:147] op_sel:[0,1] op_sel_hi:[1,0]
	ds_read2_b32 v[146:147], v145 offset0:125 offset1:126
	s_waitcnt lgkmcnt(0)
	v_pk_add_f32 v[86:87], v[86:87], v[146:147] op_sel:[0,1] op_sel_hi:[1,0]
	ds_read2_b32 v[146:147], v145 offset0:93 offset1:94
	s_waitcnt lgkmcnt(0)
	v_pk_add_f32 v[102:103], v[102:103], v[146:147] op_sel:[0,1] op_sel_hi:[1,0]
	ds_read2_b32 v[146:147], v145 offset0:119 offset1:120
	s_waitcnt lgkmcnt(0)
	v_pk_add_f32 v[88:89], v[88:89], v[146:147] op_sel:[0,1] op_sel_hi:[1,0]
	ds_read2_b32 v[146:147], v145 offset0:87 offset1:88
	s_waitcnt lgkmcnt(0)
	v_pk_add_f32 v[104:105], v[104:105], v[146:147] op_sel:[0,1] op_sel_hi:[1,0]
	ds_read2_b32 v[146:147], v145 offset0:117 offset1:118
	s_waitcnt lgkmcnt(0)
	v_pk_add_f32 v[90:91], v[90:91], v[146:147] op_sel:[0,1] op_sel_hi:[1,0]
	ds_read2_b32 v[146:147], v145 offset0:85 offset1:86
	s_waitcnt lgkmcnt(0)
	v_pk_add_f32 v[106:107], v[106:107], v[146:147] op_sel:[0,1] op_sel_hi:[1,0]
	ds_read2_b32 v[146:147], v145 offset0:111 offset1:112
	s_waitcnt lgkmcnt(0)
	v_pk_add_f32 v[92:93], v[92:93], v[146:147] op_sel:[0,1] op_sel_hi:[1,0]
	ds_read2_b32 v[146:147], v145 offset0:79 offset1:80
	s_waitcnt lgkmcnt(0)
	v_pk_add_f32 v[108:109], v[108:109], v[146:147] op_sel:[0,1] op_sel_hi:[1,0]
	ds_read2_b32 v[146:147], v145 offset0:109 offset1:110
	s_waitcnt lgkmcnt(0)
	v_pk_add_f32 v[94:95], v[94:95], v[146:147] op_sel:[0,1] op_sel_hi:[1,0]
	ds_read2_b32 v[146:147], v145 offset0:77 offset1:78
	s_waitcnt lgkmcnt(0)
	v_pk_add_f32 v[110:111], v[110:111], v[146:147] op_sel:[0,1] op_sel_hi:[1,0]
	ds_read2_b32 v[146:147], v145 offset0:103 offset1:104
	s_waitcnt lgkmcnt(0)
	v_pk_add_f32 v[96:97], v[96:97], v[146:147] op_sel:[0,1] op_sel_hi:[1,0]
	ds_read2_b32 v[146:147], v145 offset0:71 offset1:72
	s_waitcnt lgkmcnt(0)
	v_pk_add_f32 v[112:113], v[112:113], v[146:147] op_sel:[0,1] op_sel_hi:[1,0]
	ds_read2_b32 v[146:147], v145 offset0:101 offset1:102
	s_waitcnt lgkmcnt(0)
	v_pk_add_f32 v[98:99], v[98:99], v[146:147] op_sel:[0,1] op_sel_hi:[1,0]
	ds_read2_b32 v[146:147], v145 offset0:69 offset1:70
	s_waitcnt lgkmcnt(0)
	v_pk_add_f32 v[114:115], v[114:115], v[146:147] op_sel:[0,1] op_sel_hi:[1,0]
	s_branch .LBB0_1591
	s_cmp_eq_u32 s60, 2
	s_cselect_b64 vcc, -1, 0
	s_cmp_eq_u32 s60, 1
	s_cselect_b64 s[12:13], -1, 0
	s_cmp_eq_u32 s60, 3
	s_cselect_b32 s40, 64, 0
	v_mov_b32_e32 v145, s40
	s_cselect_b32 s40, -1, 63
	s_cmp_eq_u32 s47, 2
	v_cndmask_b32_e32 v145, v145, v138, vcc
	v_mov_b32_e32 v146, s40
	s_cselect_b64 vcc, -1, 0
	s_cmp_eq_u32 s47, 1
	v_cndmask_b32_e64 v146, v146, v138, s[12:13]
	s_cselect_b64 s[12:13], -1, 0
	s_cmp_eq_u32 s47, 3
	s_cselect_b32 s40, 64, 0
	v_mov_b32_e32 v147, s40
	s_cselect_b32 s40, -1, 63
	v_sub_u32_e32 v145, v145, v141
	v_sub_u32_e32 v146, v146, v141
	v_mov_b32_e32 v148, s40
	v_cndmask_b32_e32 v147, v147, v138, vcc
	v_cndmask_b32_e64 v148, v148, v138, s[12:13]
	v_cmp_lt_i32_e32 vcc, 0, v145
	v_cmp_gt_i32_e64 s[12:13], 0, v146
	v_sub_u32_e32 v147, v147, v141
	v_sub_u32_e32 v148, v148, v141
	s_or_b64 vcc, vcc, s[12:13]
	v_cndmask_b32_e32 v84, v84, v234, vcc
	v_cmp_lt_i32_e32 vcc, 0, v147
	v_cmp_gt_i32_e64 s[12:13], 0, v148
	s_or_b64 vcc, vcc, s[12:13]
	v_cndmask_b32_e32 v100, v100, v234, vcc
	v_cmp_lt_i32_e32 vcc, 1, v145
	v_cmp_gt_i32_e64 s[12:13], 1, v146
	s_or_b64 vcc, vcc, s[12:13]
	v_cndmask_b32_e32 v85, v85, v234, vcc
	v_cmp_lt_i32_e32 vcc, 1, v147
	v_cmp_gt_i32_e64 s[12:13], 1, v148
	s_or_b64 vcc, vcc, s[12:13]
	v_cndmask_b32_e32 v101, v101, v234, vcc
	v_cmp_lt_i32_e32 vcc, 2, v145
	v_cmp_gt_i32_e64 s[12:13], 2, v146
	s_or_b64 vcc, vcc, s[12:13]
	v_cndmask_b32_e32 v86, v86, v234, vcc
	v_cmp_lt_i32_e32 vcc, 2, v147
	v_cmp_gt_i32_e64 s[12:13], 2, v148
	s_or_b64 vcc, vcc, s[12:13]
	v_cndmask_b32_e32 v102, v102, v234, vcc
	v_cmp_lt_i32_e32 vcc, 3, v145
	v_cmp_gt_i32_e64 s[12:13], 3, v146
	s_or_b64 vcc, vcc, s[12:13]
	v_cndmask_b32_e32 v87, v87, v234, vcc
	v_cmp_lt_i32_e32 vcc, 3, v147
	v_cmp_gt_i32_e64 s[12:13], 3, v148
	s_or_b64 vcc, vcc, s[12:13]
	v_cndmask_b32_e32 v103, v103, v234, vcc
	v_cmp_lt_i32_e32 vcc, 8, v145
	v_cmp_gt_i32_e64 s[12:13], 8, v146
	s_or_b64 vcc, vcc, s[12:13]
	v_cndmask_b32_e32 v88, v88, v234, vcc
	v_cmp_lt_i32_e32 vcc, 8, v147
	v_cmp_gt_i32_e64 s[12:13], 8, v148
	s_or_b64 vcc, vcc, s[12:13]
	v_cndmask_b32_e32 v104, v104, v234, vcc
	v_cmp_lt_i32_e32 vcc, 9, v145
	v_cmp_gt_i32_e64 s[12:13], 9, v146
	s_or_b64 vcc, vcc, s[12:13]
	v_cndmask_b32_e32 v89, v89, v234, vcc
	v_cmp_lt_i32_e32 vcc, 9, v147
	v_cmp_gt_i32_e64 s[12:13], 9, v148
	s_or_b64 vcc, vcc, s[12:13]
	v_cndmask_b32_e32 v105, v105, v234, vcc
	v_cmp_lt_i32_e32 vcc, 10, v145
	v_cmp_gt_i32_e64 s[12:13], 10, v146
	s_or_b64 vcc, vcc, s[12:13]
	v_cndmask_b32_e32 v90, v90, v234, vcc
	v_cmp_lt_i32_e32 vcc, 10, v147
	v_cmp_gt_i32_e64 s[12:13], 10, v148
	s_or_b64 vcc, vcc, s[12:13]
	v_cndmask_b32_e32 v106, v106, v234, vcc
	v_cmp_lt_i32_e32 vcc, 11, v145
	v_cmp_gt_i32_e64 s[12:13], 11, v146
	s_or_b64 vcc, vcc, s[12:13]
	v_cndmask_b32_e32 v91, v91, v234, vcc
	v_cmp_lt_i32_e32 vcc, 11, v147
	v_cmp_gt_i32_e64 s[12:13], 11, v148
	s_or_b64 vcc, vcc, s[12:13]
	v_cndmask_b32_e32 v107, v107, v234, vcc
	v_cmp_lt_i32_e32 vcc, 16, v145
	v_cmp_gt_i32_e64 s[12:13], 16, v146
	s_or_b64 vcc, vcc, s[12:13]
	v_cndmask_b32_e32 v92, v92, v234, vcc
	v_cmp_lt_i32_e32 vcc, 16, v147
	v_cmp_gt_i32_e64 s[12:13], 16, v148
	s_or_b64 vcc, vcc, s[12:13]
	v_cndmask_b32_e32 v108, v108, v234, vcc
	v_cmp_lt_i32_e32 vcc, 17, v145
	v_cmp_gt_i32_e64 s[12:13], 17, v146
	s_or_b64 vcc, vcc, s[12:13]
	v_cndmask_b32_e32 v93, v93, v234, vcc
	v_cmp_lt_i32_e32 vcc, 17, v147
	v_cmp_gt_i32_e64 s[12:13], 17, v148
	s_or_b64 vcc, vcc, s[12:13]
	v_cndmask_b32_e32 v109, v109, v234, vcc
	v_cmp_lt_i32_e32 vcc, 18, v145
	v_cmp_gt_i32_e64 s[12:13], 18, v146
	s_or_b64 vcc, vcc, s[12:13]
	v_cndmask_b32_e32 v94, v94, v234, vcc
	v_cmp_lt_i32_e32 vcc, 18, v147
	v_cmp_gt_i32_e64 s[12:13], 18, v148
	s_or_b64 vcc, vcc, s[12:13]
	v_cndmask_b32_e32 v110, v110, v234, vcc
	v_cmp_lt_i32_e32 vcc, 19, v145
	v_cmp_gt_i32_e64 s[12:13], 19, v146
	s_or_b64 vcc, vcc, s[12:13]
	v_cndmask_b32_e32 v95, v95, v234, vcc
	v_cmp_lt_i32_e32 vcc, 19, v147
	v_cmp_gt_i32_e64 s[12:13], 19, v148
	s_or_b64 vcc, vcc, s[12:13]
	v_cndmask_b32_e32 v111, v111, v234, vcc
	v_cmp_lt_i32_e32 vcc, 24, v145
	v_cmp_gt_i32_e64 s[12:13], 24, v146
	s_or_b64 vcc, vcc, s[12:13]
	v_cndmask_b32_e32 v96, v96, v234, vcc
	v_cmp_lt_i32_e32 vcc, 24, v147
	v_cmp_gt_i32_e64 s[12:13], 24, v148
	s_or_b64 vcc, vcc, s[12:13]
	v_cndmask_b32_e32 v112, v112, v234, vcc
	v_cmp_lt_i32_e32 vcc, 25, v145
	v_cmp_gt_i32_e64 s[12:13], 25, v146
	s_or_b64 vcc, vcc, s[12:13]
	v_cndmask_b32_e32 v97, v97, v234, vcc
	v_cmp_lt_i32_e32 vcc, 25, v147
	v_cmp_gt_i32_e64 s[12:13], 25, v148
	s_or_b64 vcc, vcc, s[12:13]
	v_cndmask_b32_e32 v113, v113, v234, vcc
	v_cmp_lt_i32_e32 vcc, 26, v145
	v_cmp_gt_i32_e64 s[12:13], 26, v146
	s_or_b64 vcc, vcc, s[12:13]
	v_cndmask_b32_e32 v98, v98, v234, vcc
	v_cmp_lt_i32_e32 vcc, 26, v147
	v_cmp_gt_i32_e64 s[12:13], 26, v148
	s_or_b64 vcc, vcc, s[12:13]
	v_cndmask_b32_e32 v114, v114, v234, vcc
	v_cmp_lt_i32_e32 vcc, 27, v145
	v_cmp_gt_i32_e64 s[12:13], 27, v146
	s_or_b64 vcc, vcc, s[12:13]
	v_cndmask_b32_e32 v99, v99, v234, vcc
	v_cmp_lt_i32_e32 vcc, 27, v147
	v_cmp_gt_i32_e64 s[12:13], 27, v148
	s_or_b64 vcc, vcc, s[12:13]
	v_cndmask_b32_e32 v115, v115, v234, vcc

.LBB0_1608:
	s_or_b64 exec, exec, s[10:11]
	s_lshl_b32 s10, s83, 11
	s_lshl_b32 s7, s82, 8
	v_and_b32_e32 v156, 31, v4
	s_add_i32 s7, s10, s7
	s_ashr_i32 s51, s36, 6
	v_or_b32_e32 v2, s7, v156
	v_lshl_add_u32 v154, s51, 5, v2
	v_mov_b64_e32 v[6:7], s[20:21]
	s_movk_i32 s7, 0x300
	v_bfe_u32 v18, v4, 5, 1
	v_mad_i64_i32 v[6:7], s[12:13], v154, s7, v[6:7]
	s_mul_i32 s48, s6, 0x60
	v_lshl_add_u64 v[6:7], s[48:49], 1, v[6:7]
	v_lshlrev_b32_e32 v2, 4, v18
	v_lshl_add_u64 v[6:7], v[6:7], 0, v[2:3]
	global_load_dwordx4 v[130:133], v[6:7], off
	global_load_dwordx4 v[134:137], v[6:7], off offset:32
	global_load_dwordx4 v[138:141], v[6:7], off offset:64
	global_load_dwordx4 v[142:145], v[6:7], off offset:96
	global_load_dwordx4 v[146:149], v[6:7], off offset:128
	global_load_dwordx4 v[150:153], v[6:7], off offset:160
	s_barrier
	s_waitcnt vmcnt(0)
	s_waitcnt vmcnt(5)
	s_waitcnt vmcnt(4)
	s_waitcnt vmcnt(3)
	s_waitcnt vmcnt(2)
	s_waitcnt vmcnt(1)
	s_waitcnt vmcnt(0)
	s_and_saveexec_b64 s[12:13], s[4:5]
	v_mov_b32_e32 v2, s69
	ds_write_b32 v2, v5
	s_or_b64 exec, exec, s[12:13]
	s_ashr_i32 s11, s10, 31
	s_mul_i32 s5, s10, 0x300
	v_readlane_b32 s7, v255, 30
	s_mul_hi_i32 s4, s10, 0x300
	s_add_u32 s7, s7, s5
	v_readlane_b32 s5, v255, 32
	s_addc_u32 s12, s5, s4
	s_lshl_b64 s[4:5], s[10:11], 9
	v_readlane_b32 s10, v255, 25
	s_add_u32 s4, s10, s4
	v_readlane_b32 s10, v255, 26
	s_addc_u32 s5, s10, s5
	s_lshl_b32 s10, s6, 7
	s_add_u32 s10, s4, s10
	s_addc_u32 s11, s5, 0
	s_lshl_b32 s34, s51, 4
	s_lshl_b64 s[4:5], s[48:49], 1
	s_add_u32 s4, s7, s4
	s_addc_u32 s5, s12, s5
	s_ashr_i32 s7, s34, 31
	s_add_u32 s12, s4, s34
	v_and_b32_e32 v19, 63, v4
	s_addc_u32 s13, s5, s7
	s_lshl_b32 s37, s51, 10
	v_mul_u32_u24_e32 v157, 0x300, v19
	s_add_i32 s7, s37, s68
	s_mov_b32 m0, s7
	s_nop 0
	global_load_lds_dwordx4 v157, s[12:13]
	s_bfe_u32 s4, s36, 0x20006
	s_or_b32 s35, s4, 8
	s_sub_i32 s4, s35, s51
	s_lshl_b32 s44, s4, 4
	s_ashr_i32 s45, s44, 31
	s_add_u32 s4, s12, s44
	s_addc_u32 s5, s13, s45
	s_lshl_b32 s36, s35, 10
	s_add_i32 s48, s36, s68
	s_mov_b32 m0, s48
	s_nop 0
	global_load_lds_dwordx4 v157, s[4:5]
	s_add_u32 s4, s12, 0xc000
	s_addc_u32 s5, s13, 0
	s_add_i32 s35, s37, s84
	v_lshrrev_b32_e32 v2, 2, v19
	s_mov_b32 m0, s35
	s_nop 0
	global_load_lds_dwordx4 v157, s[4:5]
	s_add_u32 s4, s4, s44
	v_lshlrev_b32_e32 v4, 3, v19
	v_and_or_b32 v2, s34, 48, v2
	s_addc_u32 s5, s5, s45
	s_andn2_b32 s34, s34, 63
	v_and_b32_e32 v20, 24, v4
	s_add_i32 s35, s36, s84
	s_mov_b32 m0, s35
	s_nop 0
	global_load_lds_dwordx4 v157, s[4:5]
	s_ashr_i32 s4, s34, 31
	v_lshlrev_b32_e32 v4, 1, v20
	s_add_u32 s34, s10, s34
	v_lshl_or_b32 v158, v2, 9, v4
	s_addc_u32 s35, s11, s4
	s_add_i32 s50, s37, s78
	s_mov_b32 m0, s50
	s_nop 0
	global_load_lds_dwordx4 v158, s[34:35]
	s_add_u32 s4, s12, 0x18000
	s_addc_u32 s5, s13, 0
	s_add_i32 s10, s37, s77
	s_mov_b32 m0, s10
	s_nop 0
	global_load_lds_dwordx4 v157, s[4:5]
	s_add_u32 s4, s4, s44
	s_addc_u32 s5, s5, s45
	s_add_i32 s10, s36, s77
	s_mov_b32 m0, s10
	s_nop 0
	global_load_lds_dwordx4 v157, s[4:5]
	s_add_u32 s4, s34, 0x8000
	s_addc_u32 s5, s35, 0
	s_add_i32 s10, s7, 0xe000
	s_mov_b32 m0, s10
	s_nop 0
	global_load_lds_dwordx4 v158, s[4:5]
	s_add_u32 s4, s12, 0x24000
	s_addc_u32 s5, s13, 0
	s_add_i32 s10, s37, s85
	s_mov_b32 m0, s10
	s_nop 0
	global_load_lds_dwordx4 v157, s[4:5]
	s_add_u32 s4, s4, s44
	s_addc_u32 s5, s5, s45
	s_add_i32 s10, s36, s85
	s_mov_b32 m0, s10
	s_nop 0
	global_load_lds_dwordx4 v157, s[4:5]
	s_add_u32 s4, s34, 0x10000
	s_addc_u32 s5, s35, 0
	s_add_i32 s10, s7, 0x10000
	s_mov_b32 m0, s10
	s_nop 0
	global_load_lds_dwordx4 v158, s[4:5]
	s_waitcnt vmcnt(6) lgkmcnt(0)
	s_barrier
	s_lshl_b32 s4, s82, 3
	s_add_i32 s51, s51, s4
	s_cmp_gt_i32 s51, -1
	s_mov_b64 s[4:5], -1
	v_lshlrev_b32_e32 v2, 4, v156
	s_cbranch_scc1 .LBB0_1612
	v_lshlrev_b32_e32 v22, 4, v156
	s_mov_b64 s[4:5], 0

.LBB0_1640:
	s_or_b64 exec, exec, s[10:11]
	s_ashr_i32 s13, s12, 31
	s_lshl_b32 s47, s33, 4
	s_lshl_b64 s[4:5], s[12:13], 9
	s_add_u32 s43, s19, s4
	s_addc_u32 s46, s80, s5
	s_cmp_eq_u32 s82, 0
	s_cselect_b64 s[10:11], -1, 0
	s_cmp_lg_u32 s82, 0
	s_cselect_b64 s[4:5], -1, 0
	s_ashr_i32 s48, s47, 31
	s_add_u32 s12, s43, s47
	s_addc_u32 s13, s46, s48
	s_lshl_b32 s35, s33, 10
	v_lshlrev_b32_e32 v172, 9, v21
	s_add_i32 s33, s35, s68
	s_mov_b32 m0, s33
	s_nop 0
	global_load_lds_dwordx4 v172, s[12:13]
	s_and_b64 vcc, exec, s[10:11]
	s_cbranch_vccnz .LBB0_1642
	s_add_u32 s34, s43, s47
	s_addc_u32 s37, s46, s48
	s_add_u32 s36, s34, 0x8000
	s_addc_u32 s37, s37, 0
	s_add_i32 s34, s35, s71
	s_mov_b32 m0, s34
	s_nop 0
	global_load_lds_dwordx4 v172, s[36:37]
.LBB0_1642:
	s_and_b64 s[10:11], exec, s[10:11]
	s_cselect_b32 s44, 1, 2
	s_cmp_gt_u32 s44, s82
	s_cselect_b64 s[10:11], -1, 0
	s_cmp_le_u32 s44, s82
	s_cselect_b64 s[36:37], -1, 0
	s_cmp_lg_u64 s[36:37], 0
	s_addc_u32 s34, s44, 0
	s_and_b32 s50, s47, 0xffffffc0
	s_ashr_i32 s51, s50, 31
	s_waitcnt vmcnt(0)
	v_lshlrev_b32_e32 v5, 3, v21
	s_add_u32 s36, s43, s50
	v_lshrrev_b32_e32 v4, 2, v21
	v_and_b32_e32 v20, 24, v5
	s_addc_u32 s37, s46, s51
	v_and_or_b32 v4, s47, 48, v4
	v_lshlrev_b32_e32 v5, 1, v20
	s_add_u32 s36, s36, 0x80
	v_lshl_or_b32 v173, v4, 9, v5
	s_addc_u32 s37, s37, 0
	s_add_i32 s45, s35, s72
	s_mov_b32 m0, s45
	s_nop 0
	global_load_lds_dwordx4 v173, s[36:37]
	s_cmp_gt_u32 s34, s82
	s_mov_b64 s[38:39], -1
	s_cbranch_scc1 .LBB0_1644
	s_add_u32 s38, s43, s47
	s_addc_u32 s39, s46, s48
	s_add_u32 s38, s38, 0x10000
	s_addc_u32 s39, s39, 0
	s_add_i32 s52, s35, s73
	s_mov_b32 m0, s52
	s_nop 0
	global_load_lds_dwordx4 v172, s[38:39]
	s_add_u32 s52, s43, s50
	s_addc_u32 s53, s46, s51
	s_add_u32 s38, s52, 0x8080
	s_addc_u32 s39, s53, 0
	s_add_i32 s54, s35, s76
	s_mov_b32 m0, s54
	s_nop 0
	global_load_lds_dwordx4 v173, s[38:39]
	s_lshl_b32 s38, s34, 15
	s_add_u32 s38, s43, s38
	s_addc_u32 s39, s46, 0
	s_add_u32 s38, s38, s47
	s_addc_u32 s39, s39, s48
	s_add_i32 s54, s35, s77
	s_mov_b32 m0, s54
	s_nop 0
	global_load_lds_dwordx4 v172, s[38:39]
	s_add_u32 s38, s52, 0x10080
	s_addc_u32 s39, s53, 0
	s_add_i32 s52, s35, s78
	s_mov_b32 m0, s52
	s_nop 0
	global_load_lds_dwordx4 v173, s[38:39]
	s_waitcnt vmcnt(4) lgkmcnt(0)
	s_barrier
	s_mov_b64 s[38:39], 0
.LBB0_1644:
	s_andn2_b64 vcc, exec, s[38:39]
	s_cbranch_vccnz .LBB0_1652
	s_mov_b64 s[38:39], -1
	s_and_b64 vcc, exec, s[10:11]
	s_cbranch_vccz .LBB0_1649
	s_andn2_b64 vcc, exec, s[4:5]
	s_cbranch_vccnz .LBB0_1648
	s_add_u32 s4, s43, s50
	s_addc_u32 s5, s46, s51
	s_add_u32 s4, s4, 0x8080
	s_addc_u32 s5, s5, 0
	s_add_i32 s10, s35, s76
	s_mov_b32 m0, s10
	s_nop 0
	global_load_lds_dwordx4 v173, s[4:5]

.LBB0_1649:
	s_andn2_b64 vcc, exec, s[38:39]
	s_cbranch_vccnz .LBB0_1651
	s_add_u32 s4, s43, s47
	s_addc_u32 s5, s46, s48
	s_add_u32 s4, s4, 0x10000
	s_addc_u32 s5, s5, 0
	s_add_i32 s10, s35, s73
	s_mov_b32 m0, s10
	s_nop 0
	global_load_lds_dwordx4 v172, s[4:5]
	s_add_u32 s10, s43, s50
	s_addc_u32 s11, s46, s51
	s_add_u32 s4, s10, 0x8080
	s_addc_u32 s5, s11, 0
	s_add_i32 s38, s35, s76
	s_mov_b32 m0, s38
	s_nop 0
	global_load_lds_dwordx4 v173, s[4:5]
	s_add_u32 s4, s10, 0x10080
	s_addc_u32 s5, s11, 0
	s_add_i32 s10, s35, s78
	s_mov_b32 m0, s10
	s_nop 0
	global_load_lds_dwordx4 v173, s[4:5]

.LBB0_1655:
	s_cmp_le_i32 s34, s82
	s_cselect_b64 s[4:5], -1, 0
	s_cmp_lg_u64 s[4:5], 0
	s_addc_u32 s38, s34, 0
	s_add_i32 s10, s53, -1
	s_and_b32 s47, s10, 3
	s_cmp_le_i32 s38, s82
	s_cselect_b64 s[40:41], -1, 0
	s_cmp_gt_i32 s38, s82
	s_cselect_b64 s[42:43], -1, 0
	s_mov_b64 s[10:11], -1
	s_and_b64 vcc, exec, s[42:43]
	s_cbranch_vccz .LBB0_1659
	s_andn2_b64 vcc, exec, s[4:5]
	s_cbranch_vccnz .LBB0_1658
	s_ashr_i32 s35, s34, 31
	s_lshl_b64 s[4:5], s[34:35], 15
	s_add_u32 s4, s36, s4
	s_addc_u32 s5, s37, s5
	s_lshl_b32 s10, s47, 13
	s_add_i32 s10, s10, s45
	s_mov_b32 m0, s10
	s_nop 0
	global_load_lds_dwordx4 v173, s[4:5]

.LBB0_1659:
	s_andn2_b64 vcc, exec, s[10:11]
	s_cbranch_vccnz .LBB0_1661
	s_ashr_i32 s39, s38, 31
	s_lshl_b64 s[4:5], s[38:39], 15
	s_add_u32 s4, s12, s4
	s_addc_u32 s5, s13, s5
	s_lshl_b32 s10, s52, 13
	s_ashr_i32 s35, s34, 31
	s_add_i32 s10, s10, s33
	s_mov_b32 m0, s10
	s_nop 0
	global_load_lds_dwordx4 v172, s[4:5]
	s_lshl_b64 s[4:5], s[34:35], 15
	s_add_u32 s4, s36, s4
	s_addc_u32 s5, s37, s5
	s_lshl_b32 s10, s47, 13
	s_add_i32 s10, s10, s45
	s_mov_b32 m0, s10
	s_nop 0
	global_load_lds_dwordx4 v173, s[4:5]

.LBB0_1681:
	v_cndmask_b32_e64 v116, 0, 1, s[40:41]
	s_nop 0
	v_readfirstlane_b32 s4, v116
	s_add_i32 s42, s38, s4
	s_cmp_le_i32 s42, s82
	s_cselect_b64 s[50:51], -1, 0
	s_cmp_gt_i32 s42, s82
	s_mov_b64 s[4:5], -1
	s_cbranch_scc1 .LBB0_1683
	s_ashr_i32 s43, s42, 31
	s_lshl_b64 s[4:5], s[42:43], 15
	s_add_u32 s4, s12, s4
	s_addc_u32 s5, s13, s5
	s_lshl_b32 s10, s35, 13
	s_ashr_i32 s39, s38, 31
	s_add_i32 s10, s10, s33
	s_mov_b32 m0, s10
	s_nop 0
	global_load_lds_dwordx4 v172, s[4:5]
	s_lshl_b64 s[4:5], s[38:39], 15
	s_add_u32 s4, s36, s4
	s_addc_u32 s5, s37, s5
	s_lshl_b32 s10, s53, 13
	s_add_i32 s10, s10, s45
	s_mov_b32 m0, s10
	s_nop 0
	global_load_lds_dwordx4 v173, s[4:5]
	s_mov_b64 s[4:5], 0
.LBB0_1683:
	s_andn2_b64 vcc, exec, s[4:5]
	s_cbranch_vccnz .LBB0_1686
	s_andn2_b64 vcc, exec, s[40:41]
	s_cbranch_vccnz .LBB0_1686
	s_ashr_i32 s39, s38, 31
	s_lshl_b64 s[4:5], s[38:39], 15
	s_add_u32 s4, s36, s4
	s_addc_u32 s5, s37, s5
	s_lshl_b32 s10, s53, 13
	s_add_i32 s10, s10, s45
	s_mov_b32 m0, s10
	s_nop 0
	global_load_lds_dwordx4 v173, s[4:5]

.LBB0_1755:
	s_ashr_i32 s35, s34, 31
	s_lshl_b32 s50, s52, 4
	s_lshl_b64 s[10:11], s[34:35], 9
	s_add_u32 s5, s88, s10
	s_addc_u32 s10, s89, s11
	s_lshl_b32 s7, s48, 1
	s_add_u32 s51, s5, s7
	s_addc_u32 s55, s10, 0
	s_ashr_i32 s5, s4, 31
	s_lshl_b64 s[46:47], s[4:5], 15
	s_add_u32 s10, s51, s46
	s_addc_u32 s11, s55, s47
	s_ashr_i32 s5, s50, 31
	s_add_u32 s58, s10, s50
	s_addc_u32 s59, s11, s5
	s_lshl_b32 s56, s52, 10
	v_lshlrev_b32_e32 v185, 9, v19
	s_add_i32 s48, s56, s68
	s_mov_b32 m0, s48
	s_nop 0
	global_load_lds_dwordx4 v185, s[58:59]
	v_cndmask_b32_e64 v2, 0, 1, s[42:43]
	v_cmp_ne_u32_e64 s[10:11], 1, v2
	s_andn2_b64 vcc, exec, s[42:43]
	s_cbranch_vccnz .LBB0_1757
	s_ashr_i32 s37, s36, 31
	s_lshl_b64 s[42:43], s[36:37], 15
	s_add_u32 s13, s51, s42
	s_addc_u32 s37, s55, s43
	s_add_u32 s42, s13, s50
	s_addc_u32 s43, s37, s5
	s_add_i32 s13, s56, s71
	s_mov_b32 m0, s13
	s_nop 0
	global_load_lds_dwordx4 v185, s[42:43]
.LBB0_1757:
	s_lshl_b64 s[34:35], s[34:35], 8
	s_lshl_b64 s[34:35], s[34:35], 1
	s_add_u32 s13, s92, s34
	s_addc_u32 s34, s93, s35
	s_add_u32 s42, s13, s7
	s_addc_u32 s43, s34, 0
	s_add_u32 s7, s42, s46
	v_lshlrev_b32_e32 v4, 3, v19
	s_addc_u32 s13, s43, s47
	s_and_b32 s46, s50, 0xffffffc0
	v_lshrrev_b32_e32 v2, 2, v19
	v_and_b32_e32 v20, 24, v4
	s_ashr_i32 s47, s46, 31
	v_and_or_b32 v2, s50, 48, v2
	v_lshlrev_b32_e32 v4, 1, v20
	s_add_u32 s34, s7, s46
	v_lshl_or_b32 v186, v2, 9, v4
	s_addc_u32 s35, s13, s47
	s_add_i32 s54, s56, s72
	s_mov_b32 m0, s54
	s_nop 0
	global_load_lds_dwordx4 v186, s[34:35]
	s_cmp_gt_i32 s12, s45
	s_mov_b64 s[34:35], -1
	s_cbranch_scc1 .LBB0_1759
	s_ashr_i32 s7, s6, 31
	s_lshl_b64 s[34:35], s[6:7], 15
	s_add_u32 s7, s51, s34
	s_addc_u32 s13, s55, s35
	s_add_u32 s58, s7, s50
	s_addc_u32 s59, s13, s5
	s_ashr_i32 s37, s36, 31
	s_add_i32 s7, s56, s73
	s_mov_b32 m0, s7
	s_nop 0
	global_load_lds_dwordx4 v185, s[58:59]
	s_lshl_b64 s[58:59], s[36:37], 15
	s_add_u32 s7, s42, s58
	s_addc_u32 s13, s43, s59
	s_add_u32 s58, s7, s46
	s_addc_u32 s59, s13, s47
	s_add_i32 s7, s56, s76
	s_mov_b32 m0, s7
	s_nop 0
	global_load_lds_dwordx4 v186, s[58:59]
	s_ashr_i32 s13, s12, 31
	s_lshl_b64 s[58:59], s[12:13], 15
	s_add_u32 s7, s51, s58
	s_addc_u32 s13, s55, s59
	s_add_u32 s58, s7, s50
	s_addc_u32 s59, s13, s5
	s_add_i32 s7, s56, s77
	s_mov_b32 m0, s7
	s_nop 0
	global_load_lds_dwordx4 v185, s[58:59]
	s_add_u32 s7, s42, s34
	s_addc_u32 s13, s43, s35
	s_add_u32 s34, s7, s46
	s_addc_u32 s35, s13, s47
	s_add_i32 s7, s56, s78
	s_mov_b32 m0, s7
	s_nop 0
	global_load_lds_dwordx4 v186, s[34:35]
	s_waitcnt vmcnt(4) lgkmcnt(0)
	s_barrier
	s_mov_b64 s[34:35], 0
.LBB0_1759:
	s_andn2_b64 vcc, exec, s[34:35]
	s_cbranch_vccnz .LBB0_1766
	s_andn2_b64 vcc, exec, s[40:41]
	s_mov_b64 s[34:35], -1
	s_cbranch_vccnz .LBB0_1762
	s_ashr_i32 s7, s6, 31
	s_lshl_b64 s[34:35], s[6:7], 15
	s_add_u32 s7, s51, s34
	s_addc_u32 s13, s55, s35
	s_add_u32 s40, s7, s50
	s_addc_u32 s41, s13, s5
	s_ashr_i32 s37, s36, 31
	s_add_i32 s7, s56, s73
	s_mov_b32 m0, s7
	s_nop 0
	global_load_lds_dwordx4 v185, s[40:41]
	s_lshl_b64 s[40:41], s[36:37], 15
	s_add_u32 s7, s42, s40
	s_addc_u32 s13, s43, s41
	s_add_u32 s40, s7, s46
	s_addc_u32 s41, s13, s47
	s_add_i32 s7, s56, s76
	s_mov_b32 m0, s7
	s_nop 0
	global_load_lds_dwordx4 v186, s[40:41]
	s_add_u32 s7, s42, s34
	s_addc_u32 s13, s43, s35
	s_add_u32 s34, s7, s46
	s_addc_u32 s35, s13, s47
	s_add_i32 s7, s56, s78
	s_mov_b32 m0, s7
	s_nop 0
	global_load_lds_dwordx4 v186, s[34:35]
	s_mov_b64 s[34:35], 0
.LBB0_1762:
	s_andn2_b64 vcc, exec, s[34:35]
	s_cbranch_vccnz .LBB0_1765
	s_and_b64 vcc, exec, s[10:11]
	s_cbranch_vccnz .LBB0_1765
	s_ashr_i32 s37, s36, 31
	s_lshl_b64 s[10:11], s[36:37], 15
	s_add_u32 s7, s42, s10
	s_addc_u32 s11, s43, s11
	s_add_u32 s10, s7, s46
	s_addc_u32 s11, s11, s47
	s_add_i32 s7, s56, s76
	s_mov_b32 m0, s7
	s_nop 0
	global_load_lds_dwordx4 v186, s[10:11]

.LBB0_1794:
	s_cmp_le_i32 s36, s54
	s_cselect_b64 s[10:11], -1, 0
	s_cmp_lg_u64 s[10:11], 0
	s_addc_u32 s38, s36, 0
	s_add_i32 s4, s56, -1
	s_and_b32 s39, s4, 3
	s_cmp_le_i32 s38, s54
	s_cselect_b64 s[4:5], -1, 0
	s_cmp_gt_i32 s38, s54
	s_cselect_b64 s[42:43], -1, 0
	s_mov_b64 s[40:41], -1
	s_and_b64 vcc, exec, s[42:43]
	s_cbranch_vccz .LBB0_1798
	s_andn2_b64 vcc, exec, s[10:11]
	s_cbranch_vccnz .LBB0_1797
	s_ashr_i32 s37, s36, 31
	s_lshl_b64 s[10:11], s[36:37], 15
	s_add_u32 s10, s34, s10
	s_addc_u32 s11, s35, s11
	s_lshl_b32 s37, s39, 13
	s_add_i32 s37, s37, s50
	s_mov_b32 m0, s37
	s_nop 0
	global_load_lds_dwordx4 v158, s[10:11]

.LBB0_1798:
	s_andn2_b64 vcc, exec, s[40:41]
	s_cbranch_vccnz .LBB0_1800
	s_mul_i32 s10, s38, 0xc000
	s_mul_hi_i32 s11, s38, 0xc000
	s_add_u32 s10, s12, s10
	s_mul_i32 s37, s55, 0x3000
	s_addc_u32 s11, s13, s11
	s_add_i32 s40, s37, s7
	s_mov_b32 m0, s40
	s_nop 0
	global_load_lds_dwordx4 v157, s[10:11]
	s_add_u32 s10, s10, s44
	s_addc_u32 s11, s11, s45
	s_add_i32 s37, s37, s48
	s_mov_b32 m0, s37
	s_nop 0
	global_load_lds_dwordx4 v157, s[10:11]
	s_ashr_i32 s37, s36, 31
	s_lshl_b64 s[10:11], s[36:37], 15
	s_add_u32 s10, s34, s10
	s_addc_u32 s11, s35, s11
	s_lshl_b32 s37, s39, 13
	s_add_i32 s37, s37, s50
	s_mov_b32 m0, s37
	s_nop 0
	global_load_lds_dwordx4 v158, s[10:11]

.LBB0_1814:
	v_cndmask_b32_e64 v4, 0, 1, s[4:5]
	s_nop 0
	v_readfirstlane_b32 s10, v4
	s_add_i32 s57, s38, s10
	s_cmp_le_i32 s57, s54
	s_cselect_b64 s[42:43], -1, 0
	s_cmp_gt_i32 s57, s54
	s_mov_b64 s[10:11], -1
	s_cbranch_scc1 .LBB0_1816
	s_mul_i32 s10, s57, 0xc000
	s_mul_hi_i32 s11, s57, 0xc000
	s_add_u32 s10, s12, s10
	s_mulk_i32 s39, 0x3000
	s_addc_u32 s11, s13, s11
	s_add_i32 s46, s39, s7
	s_mov_b32 m0, s46
	s_nop 0
	global_load_lds_dwordx4 v157, s[10:11]
	s_add_u32 s10, s10, s44
	s_addc_u32 s11, s11, s45
	s_add_i32 s39, s39, s48
	s_mov_b32 m0, s39
	s_nop 0
	global_load_lds_dwordx4 v157, s[10:11]
	s_ashr_i32 s39, s38, 31
	s_lshl_b64 s[10:11], s[38:39], 15
	s_add_u32 s10, s34, s10
	s_addc_u32 s11, s35, s11
	s_lshl_b32 s39, s56, 13
	s_add_i32 s39, s39, s50
	s_mov_b32 m0, s39
	s_nop 0
	global_load_lds_dwordx4 v158, s[10:11]
	s_mov_b64 s[10:11], 0
.LBB0_1816:
	s_andn2_b64 vcc, exec, s[10:11]
	s_cbranch_vccnz .LBB0_1819
	s_andn2_b64 vcc, exec, s[4:5]
	s_cbranch_vccnz .LBB0_1819
	s_ashr_i32 s39, s38, 31
	s_lshl_b64 s[4:5], s[38:39], 15
	s_add_u32 s4, s34, s4
	s_addc_u32 s5, s35, s5
	s_lshl_b32 s10, s56, 13
	s_add_i32 s10, s10, s50
	s_mov_b32 m0, s10
	s_nop 0
	global_load_lds_dwordx4 v158, s[4:5]

.LBB0_1840:
	s_add_i32 s5, s57, -1
	s_and_b32 s5, s5, 3
	s_cmp_le_i32 s34, s45
	s_cselect_b64 s[38:39], -1, 0
	s_cmp_gt_i32 s34, s45
	s_mov_b64 s[40:41], -1
	s_cbranch_scc1 .LBB0_1842
	s_ashr_i32 s35, s34, 31
	s_lshl_b64 s[40:41], s[34:35], 15
	s_add_u32 s40, s7, s40
	s_addc_u32 s41, s37, s41
	s_lshl_b32 s13, s58, 13
	s_add_i32 s13, s13, s48
	s_mov_b32 m0, s13
	s_nop 0
	global_load_lds_dwordx4 v185, s[40:41]
	s_ashr_i32 s13, s12, 31
	s_lshl_b64 s[40:41], s[12:13], 15
	s_add_u32 s40, s55, s40
	s_addc_u32 s41, s56, s41
	s_lshl_b32 s13, s5, 13
	s_add_i32 s13, s13, s54
	s_mov_b32 m0, s13
	s_nop 0
	global_load_lds_dwordx4 v186, s[40:41]
	s_mov_b64 s[40:41], 0
.LBB0_1842:
	s_andn2_b64 vcc, exec, s[40:41]
	s_cbranch_vccnz .LBB0_1845
	s_andn2_b64 vcc, exec, s[10:11]
	s_cbranch_vccnz .LBB0_1845
	s_ashr_i32 s13, s12, 31
	s_lshl_b64 s[10:11], s[12:13], 15
	s_add_u32 s10, s55, s10
	s_addc_u32 s11, s56, s11
	s_lshl_b32 s5, s5, 13
	s_add_i32 s5, s5, s54
	s_mov_b32 m0, s5
	s_nop 0
	global_load_lds_dwordx4 v186, s[10:11]

.LBB0_1884:
	s_cmp_le_i32 s38, s45
	s_cselect_b64 s[40:41], -1, 0
	s_cmp_gt_i32 s38, s45
	s_mov_b64 s[4:5], -1
	s_cbranch_scc1 .LBB0_1886
	s_ashr_i32 s39, s38, 31
	s_lshl_b64 s[4:5], s[38:39], 15
	s_add_u32 s4, s7, s4
	s_addc_u32 s5, s37, s5
	s_lshl_b32 s13, s13, 13
	s_add_i32 s13, s13, s48
	s_mov_b32 m0, s13
	s_nop 0
	global_load_lds_dwordx4 v185, s[4:5]
	s_ashr_i32 s35, s34, 31
	s_lshl_b64 s[4:5], s[34:35], 15
	s_add_u32 s4, s55, s4
	s_addc_u32 s5, s56, s5
	s_lshl_b32 s13, s57, 13
	s_add_i32 s13, s13, s54
	s_mov_b32 m0, s13
	s_nop 0
	global_load_lds_dwordx4 v186, s[4:5]
	s_mov_b64 s[4:5], 0
.LBB0_1886:
	s_andn2_b64 vcc, exec, s[4:5]
	s_cbranch_vccnz .LBB0_1889
	s_and_b64 vcc, exec, s[10:11]
	s_cbranch_vccnz .LBB0_1889
	s_ashr_i32 s35, s34, 31
	s_lshl_b64 s[4:5], s[34:35], 15
	s_add_u32 s4, s55, s4
	s_addc_u32 s5, s56, s5
	s_lshl_b32 s10, s57, 13
	s_add_i32 s10, s10, s54
	s_mov_b32 m0, s10
	s_nop 0
	global_load_lds_dwordx4 v186, s[4:5]
